# baseline (speedup 1.0000x reference)
.LBB2_8:
	s_or_b64 exec, exec, s[2:3]
	v_and_b32_e32 v1, 56, v1
	v_or_b32_e32 v12, s8, v93
	s_lshl_b32 s2, s9, 1
	v_lshl_add_u32 v0, v1, 2, 0
	s_add_u32 s0, s0, s2
	v_mad_u64_u32 v[18:19], s[2:3], v12, s4, v[0:1]
	ds_read_b128 v[4:7], v18 offset:272
	ds_read_b128 v[8:11], v18 offset:288
	v_add_u32_e32 v20, s5, v12
	s_addc_u32 s1, s1, 0
	v_lshlrev_b32_e32 v2, 1, v1
	v_mov_b32_e32 v3, 0
	s_waitcnt lgkmcnt(0)
	v_cvt_pk_f16_f32 v11, v10, v11
	v_cvt_pk_f16_f32 v10, v8, v9
	v_cvt_pk_f16_f32 v9, v6, v7
	v_cvt_pk_f16_f32 v8, v4, v5
	ds_read_b128 v[4:7], v18 offset:2448
	ds_read_b128 v[12:15], v18 offset:2464
	v_ashrrev_i32_e32 v21, 31, v20
	v_lshl_add_u64 v[2:3], s[0:1], 0, v[2:3]
	v_lshlrev_b64 v[16:17], 10, v[20:21]
	v_lshl_add_u64 v[16:17], v[2:3], 0, v[16:17]
	global_store_dwordx4 v[16:17], v[8:11], off nt
	s_waitcnt lgkmcnt(1)
	v_cvt_pk_f16_f32 v7, v6, v7
	v_cvt_pk_f16_f32 v6, v4, v5
	s_waitcnt lgkmcnt(0)
	v_cvt_pk_f16_f32 v9, v14, v15
	v_cvt_pk_f16_f32 v8, v12, v13
	v_add_u32_e32 v4, 8, v20
	ds_read_b128 v[10:13], v18 offset:4624
	ds_read_b128 v[14:17], v18 offset:4640
	v_ashrrev_i32_e32 v5, 31, v4
	v_lshlrev_b64 v[4:5], 10, v[4:5]
	v_lshl_add_u64 v[4:5], v[2:3], 0, v[4:5]
	global_store_dwordx4 v[4:5], v[6:9], off nt
	s_waitcnt lgkmcnt(1)
	v_cvt_pk_f16_f32 v5, v12, v13
	v_cvt_pk_f16_f32 v4, v10, v11
	s_waitcnt lgkmcnt(0)
	v_cvt_pk_f16_f32 v7, v16, v17
	v_cvt_pk_f16_f32 v6, v14, v15
	v_add_u32_e32 v16, 16, v20
	ds_read_b128 v[8:11], v18 offset:6800
	ds_read_b128 v[12:15], v18 offset:6816
	v_ashrrev_i32_e32 v17, 31, v16
	v_lshlrev_b64 v[16:17], 10, v[16:17]
	v_lshl_add_u64 v[16:17], v[2:3], 0, v[16:17]
	global_store_dwordx4 v[16:17], v[4:7], off nt
	v_add_u32_e32 v16, 24, v20
	v_ashrrev_i32_e32 v17, 31, v16
	s_waitcnt lgkmcnt(0)
	v_cvt_pk_f16_f32 v7, v14, v15
	v_cvt_pk_f16_f32 v6, v12, v13
	v_cvt_pk_f16_f32 v5, v10, v11
	v_cvt_pk_f16_f32 v4, v8, v9
	ds_read_b128 v[8:11], v18 offset:8976
	ds_read_b128 v[12:15], v18 offset:8992
	v_lshlrev_b64 v[16:17], 10, v[16:17]
	v_lshl_add_u64 v[16:17], v[2:3], 0, v[16:17]
	global_store_dwordx4 v[16:17], v[4:7], off nt
	v_add_u32_e32 v16, 32, v20
	v_ashrrev_i32_e32 v17, 31, v16
	s_waitcnt lgkmcnt(0)
	v_cvt_pk_f16_f32 v7, v14, v15
	v_cvt_pk_f16_f32 v6, v12, v13
	v_cvt_pk_f16_f32 v5, v10, v11
	v_cvt_pk_f16_f32 v4, v8, v9
	ds_read_b128 v[8:11], v18 offset:11152
	ds_read_b128 v[12:15], v18 offset:11168
	v_lshlrev_b64 v[16:17], 10, v[16:17]
	v_lshl_add_u64 v[16:17], v[2:3], 0, v[16:17]
	global_store_dwordx4 v[16:17], v[4:7], off nt
	v_add_u32_e32 v16, 40, v20
	v_ashrrev_i32_e32 v17, 31, v16
	s_waitcnt lgkmcnt(0)
	v_cvt_pk_f16_f32 v7, v14, v15
	v_cvt_pk_f16_f32 v6, v12, v13
	v_cvt_pk_f16_f32 v5, v10, v11
	v_cvt_pk_f16_f32 v4, v8, v9
	ds_read_b128 v[8:11], v18 offset:13328
	ds_read_b128 v[12:15], v18 offset:13344
	v_lshlrev_b64 v[16:17], 10, v[16:17]
	v_lshl_add_u64 v[16:17], v[2:3], 0, v[16:17]
	global_store_dwordx4 v[16:17], v[4:7], off nt
	v_add_u32_e32 v16, 48, v20
	v_ashrrev_i32_e32 v17, 31, v16
	s_waitcnt lgkmcnt(0)
	v_cvt_pk_f16_f32 v7, v14, v15
	v_cvt_pk_f16_f32 v6, v12, v13
	v_cvt_pk_f16_f32 v5, v10, v11
	v_cvt_pk_f16_f32 v4, v8, v9
	ds_read_b128 v[8:11], v18 offset:15504
	ds_read_b128 v[12:15], v18 offset:15520
	v_lshlrev_b64 v[16:17], 10, v[16:17]
	v_lshl_add_u64 v[16:17], v[2:3], 0, v[16:17]
	global_store_dwordx4 v[16:17], v[4:7], off nt
	s_mul_i32 s0, s8, 0x110
	s_add_i32 s0, s0, 0
	s_waitcnt lgkmcnt(1)
	v_cvt_pk_f16_f32 v4, v8, v9
	v_add_u32_e32 v8, 56, v20
	v_ashrrev_i32_e32 v9, 31, v8
	v_lshlrev_b64 v[8:9], 10, v[8:9]
	v_lshlrev_b32_e32 v1, 2, v94
	s_waitcnt lgkmcnt(0)
	v_cvt_pk_f16_f32 v7, v14, v15
	v_cvt_pk_f16_f32 v6, v12, v13
	v_cvt_pk_f16_f32 v5, v10, v11
	v_lshl_add_u64 v[8:9], v[2:3], 0, v[8:9]
	v_add_u32_e32 v90, s0, v1
	global_store_dwordx4 v[8:9], v[4:7], off nt
	ds_read2_b32 v[4:5], v90 offset0:68 offset1:136
	v_add_u32_e32 v91, 0x200, v90
	ds_read2_b32 v[6:7], v91 offset0:76 offset1:144
	v_add_u32_e32 v92, 0x400, v90
	ds_read2_b32 v[8:9], v92 offset0:84 offset1:152
	v_add_u32_e32 v94, 0x600, v90
	s_waitcnt lgkmcnt(2)
	v_add_f32_e32 v68, 0, v4
	ds_read2_b32 v[10:11], v94 offset0:92 offset1:160
	v_add_f32_e32 v68, v68, v5
	v_add_u32_e32 v95, 0x800, v90
	s_waitcnt lgkmcnt(2)
	v_add_f32_e32 v68, v68, v6
	ds_read2_b32 v[12:13], v95 offset0:100 offset1:168
	v_add_f32_e32 v68, v68, v7
	v_add_u32_e32 v96, 0xa00, v90
	s_waitcnt lgkmcnt(2)
	v_add_f32_e32 v68, v68, v8
	ds_read2_b32 v[14:15], v96 offset0:108 offset1:176
	v_add_f32_e32 v68, v68, v9
	v_add_u32_e32 v97, 0xc00, v90
	s_waitcnt lgkmcnt(2)
	v_add_f32_e32 v68, v68, v10
	ds_read2_b32 v[16:17], v97 offset0:116 offset1:184
	v_add_f32_e32 v68, v68, v11
	v_add_u32_e32 v98, 0xe00, v90
	s_waitcnt lgkmcnt(2)
	v_add_f32_e32 v68, v68, v12
	ds_read2_b32 v[18:19], v98 offset0:124 offset1:192
	v_add_f32_e32 v68, v68, v13
	v_add_u32_e32 v99, 0x1000, v90
	s_waitcnt lgkmcnt(2)
	v_add_f32_e32 v68, v68, v14
	ds_read2_b32 v[20:21], v99 offset0:132 offset1:200
	v_add_f32_e32 v68, v68, v15
	s_waitcnt lgkmcnt(2)
	v_add_f32_e32 v68, v68, v16
	v_add_u32_e32 v100, 0x1400, v90
	v_add_f32_e32 v68, v68, v17
	ds_read2_b32 v[22:23], v100 offset0:12 offset1:80
	ds_read2_b32 v[24:25], v100 offset0:148 offset1:216
	s_waitcnt lgkmcnt(3)
	v_add_f32_e32 v68, v68, v18
	v_add_f32_e32 v68, v68, v19
	s_waitcnt lgkmcnt(2)
	v_add_f32_e32 v68, v68, v20
	v_add_u32_e32 v101, 0x1800, v90
	v_add_f32_e32 v68, v68, v21
	ds_read2_b32 v[26:27], v101 offset0:28 offset1:96
	ds_read2_b32 v[28:29], v101 offset0:164 offset1:232
	s_waitcnt lgkmcnt(3)
	v_add_f32_e32 v68, v68, v22
	v_add_f32_e32 v68, v68, v23
	s_waitcnt lgkmcnt(2)
	v_add_f32_e32 v68, v68, v24
	v_add_u32_e32 v102, 0x1c00, v90
	v_add_f32_e32 v68, v68, v25
	ds_read2_b32 v[30:31], v102 offset0:44 offset1:112
	ds_read2_b32 v[32:33], v102 offset0:180 offset1:248
	s_waitcnt lgkmcnt(3)
	v_add_f32_e32 v68, v68, v26
	v_add_f32_e32 v68, v68, v27
	v_add_u32_e32 v103, 0x2000, v90
	s_waitcnt lgkmcnt(2)
	v_add_f32_e32 v68, v68, v28
	ds_read2_b32 v[34:35], v103 offset0:60 offset1:128
	v_add_f32_e32 v68, v68, v29
	v_add_u32_e32 v104, 0x2200, v90
	s_waitcnt lgkmcnt(2)
	v_add_f32_e32 v68, v68, v30
	ds_read2_b32 v[36:37], v104 offset0:68 offset1:136
	v_add_f32_e32 v68, v68, v31
	v_add_u32_e32 v105, 0x2400, v90
	s_waitcnt lgkmcnt(2)
	v_add_f32_e32 v68, v68, v32
	ds_read2_b32 v[38:39], v105 offset0:76 offset1:144
	v_add_f32_e32 v68, v68, v33
	v_add_u32_e32 v106, 0x2600, v90
	s_waitcnt lgkmcnt(2)
	v_add_f32_e32 v68, v68, v34
	ds_read2_b32 v[40:41], v106 offset0:84 offset1:152
	v_add_f32_e32 v68, v68, v35
	v_add_u32_e32 v107, 0x2800, v90
	s_waitcnt lgkmcnt(2)
	v_add_f32_e32 v68, v68, v36
	ds_read2_b32 v[42:43], v107 offset0:92 offset1:160
	v_add_f32_e32 v68, v68, v37
	v_add_u32_e32 v108, 0x2a00, v90
	s_waitcnt lgkmcnt(2)
	v_add_f32_e32 v68, v68, v38
	ds_read2_b32 v[44:45], v108 offset0:100 offset1:168
	v_add_f32_e32 v68, v68, v39
	v_add_u32_e32 v109, 0x2c00, v90
	s_waitcnt lgkmcnt(2)
	v_add_f32_e32 v68, v68, v40
	ds_read2_b32 v[46:47], v109 offset0:108 offset1:176
	v_add_f32_e32 v68, v68, v41
	v_add_u32_e32 v110, 0x2e00, v90
	s_waitcnt lgkmcnt(2)
	v_add_f32_e32 v68, v68, v42
	ds_read2_b32 v[48:49], v110 offset0:116 offset1:184
	v_add_f32_e32 v68, v68, v43
	v_add_u32_e32 v111, 0x3000, v90
	s_waitcnt lgkmcnt(2)
	v_add_f32_e32 v68, v68, v44
	ds_read2_b32 v[50:51], v111 offset0:124 offset1:192
	v_add_f32_e32 v68, v68, v45
	s_waitcnt lgkmcnt(2)
	v_add_f32_e32 v68, v68, v46
	v_add_u32_e32 v112, 0x3400, v90
	v_add_f32_e32 v68, v68, v47
	ds_read2_b32 v[52:53], v112 offset0:4 offset1:72
	ds_read2_b32 v[54:55], v112 offset0:140 offset1:208
	s_waitcnt lgkmcnt(3)
	v_add_f32_e32 v68, v68, v48
	v_add_f32_e32 v68, v68, v49
	s_waitcnt lgkmcnt(2)
	v_add_f32_e32 v68, v68, v50
	v_add_u32_e32 v113, 0x3800, v90
	v_add_f32_e32 v68, v68, v51
	ds_read2_b32 v[56:57], v113 offset0:20 offset1:88
	ds_read2_b32 v[58:59], v113 offset0:156 offset1:224
	s_waitcnt lgkmcnt(3)
	v_add_f32_e32 v68, v68, v52
	v_add_f32_e32 v68, v68, v53
	s_waitcnt lgkmcnt(2)
	v_add_f32_e32 v68, v68, v54
	v_add_u32_e32 v114, 0x3c00, v90
	v_add_f32_e32 v68, v68, v55
	ds_read2_b32 v[60:61], v114 offset0:36 offset1:104
	ds_read2_b32 v[62:63], v114 offset0:172 offset1:240
	s_waitcnt lgkmcnt(3)
	v_add_f32_e32 v68, v68, v56
	v_add_f32_e32 v68, v68, v57
	v_add_u32_e32 v115, 0x4000, v90
	s_waitcnt lgkmcnt(2)
	v_add_f32_e32 v68, v68, v58
	ds_read2_b32 v[64:65], v115 offset0:52 offset1:120
	v_add_f32_e32 v68, v68, v59
	v_add_u32_e32 v116, 0x4200, v90
	s_waitcnt lgkmcnt(2)
	v_add_f32_e32 v68, v68, v60
	ds_read2_b32 v[66:67], v116 offset0:60 offset1:128
	v_add_f32_e32 v68, v68, v61
	s_waitcnt lgkmcnt(2)
	v_add_f32_e32 v68, v68, v62
	v_add_f32_e32 v68, v68, v63
	s_waitcnt lgkmcnt(1)
	v_add_f32_e32 v68, v68, v64
	v_add_f32_e32 v68, v68, v65
	s_lshl_b32 s0, s8, 2
	s_add_i32 s1, 0, 0x22110
	s_waitcnt lgkmcnt(0)
	v_add_f32_e32 v68, v68, v66
	s_add_i32 s0, s1, s0
	v_add_f32_e32 v68, v68, v67
	v_add_u32_e32 v69, s0, v1
	v_add_u32_e32 v1, s1, v1
	ds_write_b32 v69, v68
	s_waitcnt lgkmcnt(0)
	s_barrier
	ds_read2st64_b32 v[68:69], v1 offset1:1
	s_cmpk_gt_u32 s20, 0x7f
	v_cndmask_b32_e64 v117, 1.0, 0, s[6:7]
	ds_read2st64_b32 v[70:71], v1 offset0:2 offset1:3
	ds_read2st64_b32 v[88:89], v1 offset0:4 offset1:5
	ds_read_b32 v1, v1 offset:1536
	s_cselect_b64 s[0:1], -1, 0
	s_cmpk_gt_u32 s20, 0xbf
	s_waitcnt lgkmcnt(3)
	v_fma_f32 v68, v117, v68, 0
	v_cndmask_b32_e64 v117, 0, 1.0, s[0:1]
	s_cselect_b64 s[0:1], -1, 0
	s_cmpk_gt_u32 s20, 0xff
	v_fmac_f32_e32 v68, v117, v69
	v_cndmask_b32_e64 v69, 0, 1.0, s[0:1]
	s_cselect_b64 s[0:1], -1, 0
	s_cmpk_gt_u32 s20, 0x13f
	s_waitcnt lgkmcnt(2)
	v_fmac_f32_e32 v68, v69, v70
	v_cndmask_b32_e64 v69, 0, 1.0, s[0:1]
	s_cselect_b64 s[0:1], -1, 0
	s_cmpk_gt_u32 s20, 0x17f
	v_fmac_f32_e32 v68, v69, v71
	v_cndmask_b32_e64 v69, 0, 1.0, s[0:1]
	s_cselect_b64 s[0:1], -1, 0
	s_cmpk_gt_u32 s20, 0x1bf
	s_waitcnt lgkmcnt(1)
	v_fmac_f32_e32 v68, v69, v88
	v_cndmask_b32_e64 v69, 0, 1.0, s[0:1]
	s_cselect_b64 s[0:1], -1, 0
	v_fmac_f32_e32 v68, v69, v89
	v_cndmask_b32_e64 v69, 0, 1.0, s[0:1]
	s_waitcnt lgkmcnt(0)
	v_fmac_f32_e32 v68, v69, v1
	v_add_f32_e32 v1, v68, v4
	v_add_f32_e32 v4, v1, v5
	ds_write2_b32 v90, v1, v4 offset0:68 offset1:136
	v_add_f32_e32 v1, v4, v6
	v_add_f32_e32 v4, v1, v7
	ds_write2_b32 v91, v1, v4 offset0:76 offset1:144
	v_add_f32_e32 v1, v4, v8
	v_add_f32_e32 v4, v1, v9
	ds_write2_b32 v92, v1, v4 offset0:84 offset1:152
	v_add_f32_e32 v1, v4, v10
	v_add_f32_e32 v4, v1, v11
	ds_write2_b32 v94, v1, v4 offset0:92 offset1:160
	v_add_f32_e32 v1, v4, v12
	v_add_f32_e32 v4, v1, v13
	ds_write2_b32 v95, v1, v4 offset0:100 offset1:168
	v_add_f32_e32 v1, v4, v14
	v_add_f32_e32 v4, v1, v15
	ds_write2_b32 v96, v1, v4 offset0:108 offset1:176
	v_add_f32_e32 v1, v4, v16
	v_add_f32_e32 v4, v1, v17
	ds_write2_b32 v97, v1, v4 offset0:116 offset1:184
	v_add_f32_e32 v1, v4, v18
	v_add_f32_e32 v4, v1, v19
	ds_write2_b32 v98, v1, v4 offset0:124 offset1:192
	v_add_f32_e32 v1, v4, v20
	v_add_f32_e32 v4, v1, v21
	ds_write2_b32 v99, v1, v4 offset0:132 offset1:200
	v_add_f32_e32 v1, v4, v22
	v_add_f32_e32 v4, v1, v23
	ds_write2_b32 v100, v1, v4 offset0:12 offset1:80
	v_add_f32_e32 v1, v4, v24
	v_add_f32_e32 v4, v1, v25
	ds_write2_b32 v100, v1, v4 offset0:148 offset1:216
	v_add_f32_e32 v1, v4, v26
	v_add_f32_e32 v4, v1, v27
	ds_write2_b32 v101, v1, v4 offset0:28 offset1:96
	v_add_f32_e32 v1, v4, v28
	v_add_f32_e32 v4, v1, v29
	ds_write2_b32 v101, v1, v4 offset0:164 offset1:232
	v_add_f32_e32 v1, v4, v30
	v_add_f32_e32 v4, v1, v31
	ds_write2_b32 v102, v1, v4 offset0:44 offset1:112
	v_add_f32_e32 v1, v4, v32
	v_add_f32_e32 v4, v1, v33
	ds_write2_b32 v102, v1, v4 offset0:180 offset1:248
	v_add_f32_e32 v1, v4, v34
	v_add_f32_e32 v4, v1, v35
	ds_write2_b32 v103, v1, v4 offset0:60 offset1:128
	v_add_f32_e32 v1, v4, v36
	v_add_f32_e32 v4, v1, v37
	ds_write2_b32 v104, v1, v4 offset0:68 offset1:136
	v_add_f32_e32 v1, v4, v38
	v_add_f32_e32 v4, v1, v39
	ds_write2_b32 v105, v1, v4 offset0:76 offset1:144
	v_add_f32_e32 v1, v4, v40
	v_add_f32_e32 v4, v1, v41
	ds_write2_b32 v106, v1, v4 offset0:84 offset1:152
	v_add_f32_e32 v1, v4, v42
	v_add_f32_e32 v4, v1, v43
	ds_write2_b32 v107, v1, v4 offset0:92 offset1:160
	v_add_f32_e32 v1, v4, v44
	v_add_f32_e32 v4, v1, v45
	ds_write2_b32 v108, v1, v4 offset0:100 offset1:168
	v_add_f32_e32 v1, v4, v46
	v_add_f32_e32 v4, v1, v47
	ds_write2_b32 v109, v1, v4 offset0:108 offset1:176
	v_add_f32_e32 v1, v4, v48
	v_add_f32_e32 v4, v1, v49
	ds_write2_b32 v110, v1, v4 offset0:116 offset1:184
	v_add_f32_e32 v1, v4, v50
	v_add_f32_e32 v4, v1, v51
	ds_write2_b32 v111, v1, v4 offset0:124 offset1:192
	v_add_f32_e32 v1, v4, v52
	v_add_f32_e32 v4, v1, v53
	ds_write2_b32 v112, v1, v4 offset0:4 offset1:72
	v_add_f32_e32 v1, v4, v54
	v_add_f32_e32 v4, v1, v55
	ds_write2_b32 v112, v1, v4 offset0:140 offset1:208
	v_add_f32_e32 v1, v4, v56
	v_add_f32_e32 v4, v1, v57
	ds_write2_b32 v113, v1, v4 offset0:20 offset1:88
	v_add_f32_e32 v1, v4, v58
	v_add_f32_e32 v4, v1, v59
	ds_write2_b32 v113, v1, v4 offset0:156 offset1:224
	v_add_f32_e32 v1, v4, v60
	v_add_f32_e32 v4, v1, v61
	ds_write2_b32 v114, v1, v4 offset0:36 offset1:104
	v_add_f32_e32 v1, v4, v62
	v_add_f32_e32 v4, v1, v63
	ds_write2_b32 v114, v1, v4 offset0:172 offset1:240
	v_add_f32_e32 v1, v4, v64
	v_add_f32_e32 v4, v1, v65
	ds_write2_b32 v115, v1, v4 offset0:52 offset1:120
	v_add_f32_e32 v1, v4, v66
	v_add_f32_e32 v4, v1, v67
	ds_write2_b32 v116, v1, v4 offset0:60 offset1:128
	v_or_b32_e32 v1, s5, v93
	v_add_u32_e32 v4, s8, v1
	v_sub_u32_e32 v1, v87, v86
	v_mov_b32_e32 v25, 0x1ff
	v_mov_b32_e32 v26, 0x200
	v_cvt_f32_i32_e32 v1, v1
	v_med3_i32 v5, v86, 0, v25
	v_med3_i32 v10, v87, 1, v26
	v_mad_u32_u24 v5, v5, s4, v0
	v_mad_u32_u24 v18, v10, s4, v0
	s_waitcnt lgkmcnt(0)
	s_barrier
	v_med3_i32 v188, v86, 0, v25
	v_med3_i32 v189, v87, 1, v26
	v_mad_u32_u24 v188, v188, s4, v0
	v_mad_u32_u24 v189, v189, s4, v0
	ds_read_b128 v[100:103], v188
	ds_read_b128 v[104:107], v189
	ds_read_b128 v[108:111], v188 offset:16
	ds_read_b128 v[112:115], v189 offset:16
	v_med3_i32 v190, v84, 0, v25
	v_med3_i32 v191, v85, 1, v26
	v_mad_u32_u24 v190, v190, s4, v0
	v_mad_u32_u24 v191, v191, s4, v0
	ds_read_b128 v[116:119], v190
	ds_read_b128 v[120:123], v191
	ds_read_b128 v[124:127], v190 offset:16
	ds_read_b128 v[128:131], v191 offset:16
	v_med3_i32 v192, v82, 0, v25
	v_med3_i32 v193, v83, 1, v26
	v_mad_u32_u24 v192, v192, s4, v0
	v_mad_u32_u24 v193, v193, s4, v0
	ds_read_b128 v[132:135], v192
	ds_read_b128 v[136:139], v193
	ds_read_b128 v[140:143], v192 offset:16
	ds_read_b128 v[144:147], v193 offset:16
	v_med3_i32 v194, v80, 0, v25
	v_med3_i32 v195, v81, 1, v26
	v_mad_u32_u24 v194, v194, s4, v0
	v_mad_u32_u24 v195, v195, s4, v0
	ds_read_b128 v[148:151], v194
	ds_read_b128 v[152:155], v195
	ds_read_b128 v[156:159], v194 offset:16
	ds_read_b128 v[160:163], v195 offset:16
	s_mov_b64 s[0:1], 0x1000000
	v_lshl_add_u64 v[2:3], v[2:3], 0, s[0:1]
	v_sub_u32_e32 v172, v87, v86
	v_sub_u32_e32 v174, v85, v84
	v_sub_u32_e32 v176, v83, v82
	v_sub_u32_e32 v178, v81, v80
	v_sub_u32_e32 v180, v79, v78
	v_sub_u32_e32 v182, v77, v76
	v_sub_u32_e32 v184, v75, v74
	v_sub_u32_e32 v186, v73, v72
	v_cvt_f32_i32_e32 v172, v172
	v_cvt_f32_i32_e32 v174, v174
	v_cvt_f32_i32_e32 v176, v176
	v_cvt_f32_i32_e32 v178, v178
	v_cvt_f32_i32_e32 v180, v180
	v_cvt_f32_i32_e32 v182, v182
	v_cvt_f32_i32_e32 v184, v184
	v_cvt_f32_i32_e32 v186, v186
	v_rcp_iflag_f32_e32 v172, v172
	v_rcp_iflag_f32_e32 v174, v174
	v_rcp_iflag_f32_e32 v176, v176
	v_rcp_iflag_f32_e32 v178, v178
	v_rcp_iflag_f32_e32 v180, v180
	v_rcp_iflag_f32_e32 v182, v182
	v_rcp_iflag_f32_e32 v184, v184
	v_rcp_iflag_f32_e32 v186, v186
	s_waitcnt lgkmcnt(12)
	v_sub_f32_e32 v100, v104, v100
	v_sub_f32_e32 v101, v105, v101
	v_sub_f32_e32 v102, v106, v102
	v_sub_f32_e32 v103, v107, v103
	v_sub_f32_e32 v108, v112, v108
	v_sub_f32_e32 v109, v113, v109
	v_sub_f32_e32 v110, v114, v110
	v_sub_f32_e32 v111, v115, v111
	v_mov_b32_e32 v60, v4
	v_pk_mul_f32 v[100:101], v[100:101], v[172:173] op_sel_hi:[1,0]
	v_pk_mul_f32 v[102:103], v[102:103], v[172:173] op_sel_hi:[1,0]
	v_pk_mul_f32 v[108:109], v[108:109], v[172:173] op_sel_hi:[1,0]
	v_pk_mul_f32 v[110:111], v[110:111], v[172:173] op_sel_hi:[1,0]
	v_ashrrev_i32_e32 v61, 31, v60
	v_lshlrev_b64 v[60:61], 10, v[60:61]
	v_cvt_pk_f16_f32 v64, v100, v101
	v_cvt_pk_f16_f32 v65, v102, v103
	v_cvt_pk_f16_f32 v66, v108, v109
	v_cvt_pk_f16_f32 v67, v110, v111
	v_lshl_add_u64 v[60:61], v[2:3], 0, v[60:61]
	global_store_dwordx4 v[60:61], v[64:67], off nt
	v_med3_i32 v196, v78, 0, v25
	v_med3_i32 v197, v79, 1, v26
	v_mad_u32_u24 v196, v196, s4, v0
	v_mad_u32_u24 v197, v197, s4, v0
	ds_read_b128 v[100:103], v196
	ds_read_b128 v[104:107], v197
	ds_read_b128 v[108:111], v196 offset:16
	ds_read_b128 v[112:115], v197 offset:16
	s_waitcnt lgkmcnt(12)
	v_sub_f32_e32 v116, v120, v116
	v_sub_f32_e32 v117, v121, v117
	v_sub_f32_e32 v118, v122, v118
	v_sub_f32_e32 v119, v123, v119
	v_sub_f32_e32 v124, v128, v124
	v_sub_f32_e32 v125, v129, v125
	v_sub_f32_e32 v126, v130, v126
	v_sub_f32_e32 v127, v131, v127
	v_or_b32_e32 v62, 8, v4
	v_pk_mul_f32 v[116:117], v[116:117], v[174:175] op_sel_hi:[1,0]
	v_pk_mul_f32 v[118:119], v[118:119], v[174:175] op_sel_hi:[1,0]
	v_pk_mul_f32 v[124:125], v[124:125], v[174:175] op_sel_hi:[1,0]
	v_pk_mul_f32 v[126:127], v[126:127], v[174:175] op_sel_hi:[1,0]
	v_ashrrev_i32_e32 v63, 31, v62
	v_lshlrev_b64 v[62:63], 10, v[62:63]
	v_cvt_pk_f16_f32 v68, v116, v117
	v_cvt_pk_f16_f32 v69, v118, v119
	v_cvt_pk_f16_f32 v70, v124, v125
	v_cvt_pk_f16_f32 v71, v126, v127
	v_lshl_add_u64 v[62:63], v[2:3], 0, v[62:63]
	global_store_dwordx4 v[62:63], v[68:71], off nt
	v_med3_i32 v198, v76, 0, v25
	v_med3_i32 v199, v77, 1, v26
	v_mad_u32_u24 v198, v198, s4, v0
	v_mad_u32_u24 v199, v199, s4, v0
	ds_read_b128 v[116:119], v198
	ds_read_b128 v[120:123], v199
	ds_read_b128 v[124:127], v198 offset:16
	ds_read_b128 v[128:131], v199 offset:16
	s_waitcnt lgkmcnt(12)
	v_sub_f32_e32 v132, v136, v132
	v_sub_f32_e32 v133, v137, v133
	v_sub_f32_e32 v134, v138, v134
	v_sub_f32_e32 v135, v139, v135
	v_sub_f32_e32 v140, v144, v140
	v_sub_f32_e32 v141, v145, v141
	v_sub_f32_e32 v142, v146, v142
	v_sub_f32_e32 v143, v147, v143
	v_or_b32_e32 v60, 16, v4
	v_pk_mul_f32 v[132:133], v[132:133], v[176:177] op_sel_hi:[1,0]
	v_pk_mul_f32 v[134:135], v[134:135], v[176:177] op_sel_hi:[1,0]
	v_pk_mul_f32 v[140:141], v[140:141], v[176:177] op_sel_hi:[1,0]
	v_pk_mul_f32 v[142:143], v[142:143], v[176:177] op_sel_hi:[1,0]
	v_ashrrev_i32_e32 v61, 31, v60
	v_lshlrev_b64 v[60:61], 10, v[60:61]
	v_cvt_pk_f16_f32 v64, v132, v133
	v_cvt_pk_f16_f32 v65, v134, v135
	v_cvt_pk_f16_f32 v66, v140, v141
	v_cvt_pk_f16_f32 v67, v142, v143
	v_lshl_add_u64 v[60:61], v[2:3], 0, v[60:61]
	global_store_dwordx4 v[60:61], v[64:67], off nt
	v_med3_i32 v200, v74, 0, v25
	v_med3_i32 v201, v75, 1, v26
	v_mad_u32_u24 v200, v200, s4, v0
	v_mad_u32_u24 v201, v201, s4, v0
	ds_read_b128 v[132:135], v200
	ds_read_b128 v[136:139], v201
	ds_read_b128 v[140:143], v200 offset:16
	ds_read_b128 v[144:147], v201 offset:16
	s_waitcnt lgkmcnt(12)
	v_sub_f32_e32 v148, v152, v148
	v_sub_f32_e32 v149, v153, v149
	v_sub_f32_e32 v150, v154, v150
	v_sub_f32_e32 v151, v155, v151
	v_sub_f32_e32 v156, v160, v156
	v_sub_f32_e32 v157, v161, v157
	v_sub_f32_e32 v158, v162, v158
	v_sub_f32_e32 v159, v163, v159
	v_or_b32_e32 v62, 24, v4
	v_pk_mul_f32 v[148:149], v[148:149], v[178:179] op_sel_hi:[1,0]
	v_pk_mul_f32 v[150:151], v[150:151], v[178:179] op_sel_hi:[1,0]
	v_pk_mul_f32 v[156:157], v[156:157], v[178:179] op_sel_hi:[1,0]
	v_pk_mul_f32 v[158:159], v[158:159], v[178:179] op_sel_hi:[1,0]
	v_ashrrev_i32_e32 v63, 31, v62
	v_lshlrev_b64 v[62:63], 10, v[62:63]
	v_cvt_pk_f16_f32 v68, v148, v149
	v_cvt_pk_f16_f32 v69, v150, v151
	v_cvt_pk_f16_f32 v70, v156, v157
	v_cvt_pk_f16_f32 v71, v158, v159
	v_lshl_add_u64 v[62:63], v[2:3], 0, v[62:63]
	global_store_dwordx4 v[62:63], v[68:71], off nt
	v_med3_i32 v202, v72, 0, v25
	v_med3_i32 v203, v73, 1, v26
	v_mad_u32_u24 v202, v202, s4, v0
	v_mad_u32_u24 v203, v203, s4, v0
	ds_read_b128 v[148:151], v202
	ds_read_b128 v[152:155], v203
	ds_read_b128 v[156:159], v202 offset:16
	ds_read_b128 v[160:163], v203 offset:16
	s_waitcnt lgkmcnt(12)
	v_sub_f32_e32 v100, v104, v100
	v_sub_f32_e32 v101, v105, v101
	v_sub_f32_e32 v102, v106, v102
	v_sub_f32_e32 v103, v107, v103
	v_sub_f32_e32 v108, v112, v108
	v_sub_f32_e32 v109, v113, v109
	v_sub_f32_e32 v110, v114, v110
	v_sub_f32_e32 v111, v115, v111
	v_or_b32_e32 v60, 32, v4
	v_pk_mul_f32 v[100:101], v[100:101], v[180:181] op_sel_hi:[1,0]
	v_pk_mul_f32 v[102:103], v[102:103], v[180:181] op_sel_hi:[1,0]
	v_pk_mul_f32 v[108:109], v[108:109], v[180:181] op_sel_hi:[1,0]
	v_pk_mul_f32 v[110:111], v[110:111], v[180:181] op_sel_hi:[1,0]
	v_ashrrev_i32_e32 v61, 31, v60
	v_lshlrev_b64 v[60:61], 10, v[60:61]
	v_cvt_pk_f16_f32 v64, v100, v101
	v_cvt_pk_f16_f32 v65, v102, v103
	v_cvt_pk_f16_f32 v66, v108, v109
	v_cvt_pk_f16_f32 v67, v110, v111
	v_lshl_add_u64 v[60:61], v[2:3], 0, v[60:61]
	global_store_dwordx4 v[60:61], v[64:67], off nt
	s_waitcnt lgkmcnt(8)
	v_sub_f32_e32 v116, v120, v116
	v_sub_f32_e32 v117, v121, v117
	v_sub_f32_e32 v118, v122, v118
	v_sub_f32_e32 v119, v123, v119
	v_sub_f32_e32 v124, v128, v124
	v_sub_f32_e32 v125, v129, v125
	v_sub_f32_e32 v126, v130, v126
	v_sub_f32_e32 v127, v131, v127
	v_or_b32_e32 v62, 40, v4
	v_pk_mul_f32 v[116:117], v[116:117], v[182:183] op_sel_hi:[1,0]
	v_pk_mul_f32 v[118:119], v[118:119], v[182:183] op_sel_hi:[1,0]
	v_pk_mul_f32 v[124:125], v[124:125], v[182:183] op_sel_hi:[1,0]
	v_pk_mul_f32 v[126:127], v[126:127], v[182:183] op_sel_hi:[1,0]
	v_ashrrev_i32_e32 v63, 31, v62
	v_lshlrev_b64 v[62:63], 10, v[62:63]
	v_cvt_pk_f16_f32 v68, v116, v117
	v_cvt_pk_f16_f32 v69, v118, v119
	v_cvt_pk_f16_f32 v70, v124, v125
	v_cvt_pk_f16_f32 v71, v126, v127
	v_lshl_add_u64 v[62:63], v[2:3], 0, v[62:63]
	global_store_dwordx4 v[62:63], v[68:71], off nt
	s_waitcnt lgkmcnt(4)
	v_sub_f32_e32 v132, v136, v132
	v_sub_f32_e32 v133, v137, v133
	v_sub_f32_e32 v134, v138, v134
	v_sub_f32_e32 v135, v139, v135
	v_sub_f32_e32 v140, v144, v140
	v_sub_f32_e32 v141, v145, v141
	v_sub_f32_e32 v142, v146, v142
	v_sub_f32_e32 v143, v147, v143
	v_or_b32_e32 v60, 48, v4
	v_pk_mul_f32 v[132:133], v[132:133], v[184:185] op_sel_hi:[1,0]
	v_pk_mul_f32 v[134:135], v[134:135], v[184:185] op_sel_hi:[1,0]
	v_pk_mul_f32 v[140:141], v[140:141], v[184:185] op_sel_hi:[1,0]
	v_pk_mul_f32 v[142:143], v[142:143], v[184:185] op_sel_hi:[1,0]
	v_ashrrev_i32_e32 v61, 31, v60
	v_lshlrev_b64 v[60:61], 10, v[60:61]
	v_cvt_pk_f16_f32 v64, v132, v133
	v_cvt_pk_f16_f32 v65, v134, v135
	v_cvt_pk_f16_f32 v66, v140, v141
	v_cvt_pk_f16_f32 v67, v142, v143
	v_lshl_add_u64 v[60:61], v[2:3], 0, v[60:61]
	global_store_dwordx4 v[60:61], v[64:67], off nt
	s_waitcnt lgkmcnt(0)
	v_sub_f32_e32 v148, v152, v148
	v_sub_f32_e32 v149, v153, v149
	v_sub_f32_e32 v150, v154, v150
	v_sub_f32_e32 v151, v155, v151
	v_sub_f32_e32 v156, v160, v156
	v_sub_f32_e32 v157, v161, v157
	v_sub_f32_e32 v158, v162, v158
	v_sub_f32_e32 v159, v163, v159
	v_or_b32_e32 v62, 56, v4
	v_pk_mul_f32 v[148:149], v[148:149], v[186:187] op_sel_hi:[1,0]
	v_pk_mul_f32 v[150:151], v[150:151], v[186:187] op_sel_hi:[1,0]
	v_pk_mul_f32 v[156:157], v[156:157], v[186:187] op_sel_hi:[1,0]
	v_pk_mul_f32 v[158:159], v[158:159], v[186:187] op_sel_hi:[1,0]
	v_ashrrev_i32_e32 v63, 31, v62
	v_lshlrev_b64 v[62:63], 10, v[62:63]
	v_cvt_pk_f16_f32 v68, v148, v149
	v_cvt_pk_f16_f32 v69, v150, v151
	v_cvt_pk_f16_f32 v70, v156, v157
	v_cvt_pk_f16_f32 v71, v158, v159
	v_lshl_add_u64 v[62:63], v[2:3], 0, v[62:63]
	global_store_dwordx4 v[62:63], v[68:71], off nt
	s_endpgm
	.p2align	8
